# k26: grid-barrier XCD leader bumps the XCD generation word before its own acquire fence (buffer_inv) instead of after, 10 barrier sites; every workgroup still fences after observing its flag
# baseline (speedup 1.0000x reference)
; __device__ __forceinline__ unsigned xb_ld(unsigned* p)              { return __hip_atomic_load(p, __ATOMIC_RELAXED, __HIP_MEMORY_SCOPE_AGENT); }
; __device__ __forceinline__ unsigned xb_add(unsigned* p, unsigned v) { return __hip_atomic_fetch_add(p, v, __ATOMIC_RELAXED, __HIP_MEMORY_SCOPE_AGENT); }
; #define XB_SPIN(cond, bar) do { unsigned _sp = 0; while (cond) { __builtin_amdgcn_s_sleep(1); \
;     if ((++_sp & 255u) == 0u) { if (xb_ld(&(bar)[XB_TMO])) break; if (_sp > XB_SPIN_CAP) { atomicAdd(&(bar)[XB_TMO], 1u); break; } } } } while (0)
; __device__ __forceinline__ void xcd_barrier(const XcdBarrier& b) {
;     ...
;         const unsigned old = xb_add(&bar[XB_XSUB(b.x)], 1u);
;         const unsigned gen = old / nloc;
;         if (old + 1u == (gen + 1u) * nloc) {
;             __builtin_amdgcn_fence(__ATOMIC_RELEASE, "agent");
;             asm volatile("s_waitcnt vmcnt(0)" ::: "memory");
;             const unsigned og = xb_add(&bar[XB_TOP], 1u);
;             const unsigned tg = og / nx;
;             if (og + 1u == (tg + 1u) * nx) xb_add(&bar[XB_TOPGEN], 1u);
;             else XB_SPIN(xb_ld(&bar[XB_TOPGEN]) == tg, bar);
;             __builtin_amdgcn_fence(__ATOMIC_ACQUIRE, "agent");
;             xb_add(&bar[XB_XGEN(b.x)], 1u);
;             asm volatile("s_waitcnt vmcnt(0)" ::: "memory");
;         } else {
;             XB_SPIN(xb_ld(&bar[XB_XGEN(b.x)]) == gen, bar);
;             __builtin_amdgcn_fence(__ATOMIC_ACQUIRE, "agent");
;             asm volatile("s_waitcnt vmcnt(0)" ::: "memory");
;         }
.LBB0_67:
	s_or_b64 exec, exec, s[6:7]
	s_mov_b64 s[6:7], exec
	v_mbcnt_lo_u32_b32 v1, s6, 0
	v_mbcnt_hi_u32_b32 v1, s7, v1
	v_cmp_eq_u32_e32 vcc, 0, v1
	s_and_saveexec_b64 s[10:11], vcc
	s_cbranch_execz .LBB0_69
	s_bcnt1_i32_b64 s3, s[6:7]
	v_mov_b32_e32 v1, 0
	v_mov_b32_e32 v2, s3
	global_atomic_add v1, v2, s[8:9]
.LBB0_69:
	s_or_b64 exec, exec, s[10:11]
	s_waitcnt vmcnt(0)
	buffer_inv sc1
	s_waitcnt vmcnt(0)
.LBB0_70:
	s_or_b64 exec, exec, s[4:5]
	s_waitcnt lgkmcnt(0)
	s_barrier

; __device__ __forceinline__ unsigned xb_ld(unsigned* p)              { return __hip_atomic_load(p, __ATOMIC_RELAXED, __HIP_MEMORY_SCOPE_AGENT); }
; __device__ __forceinline__ unsigned xb_add(unsigned* p, unsigned v) { return __hip_atomic_fetch_add(p, v, __ATOMIC_RELAXED, __HIP_MEMORY_SCOPE_AGENT); }
; #define XB_SPIN(cond, bar) do { unsigned _sp = 0; while (cond) { __builtin_amdgcn_s_sleep(1); \
;     if ((++_sp & 255u) == 0u) { if (xb_ld(&(bar)[XB_TMO])) break; if (_sp > XB_SPIN_CAP) { atomicAdd(&(bar)[XB_TMO], 1u); break; } } } } while (0)
; __device__ __forceinline__ void xcd_barrier(const XcdBarrier& b) {
;     ...
;         const unsigned old = xb_add(&bar[XB_XSUB(b.x)], 1u);
;         const unsigned gen = old / nloc;
;         if (old + 1u == (gen + 1u) * nloc) {
;             __builtin_amdgcn_fence(__ATOMIC_RELEASE, "agent");
;             asm volatile("s_waitcnt vmcnt(0)" ::: "memory");
;             const unsigned og = xb_add(&bar[XB_TOP], 1u);
;             const unsigned tg = og / nx;
;             if (og + 1u == (tg + 1u) * nx) xb_add(&bar[XB_TOPGEN], 1u);
;             else XB_SPIN(xb_ld(&bar[XB_TOPGEN]) == tg, bar);
;             __builtin_amdgcn_fence(__ATOMIC_ACQUIRE, "agent");
;             xb_add(&bar[XB_XGEN(b.x)], 1u);
;             asm volatile("s_waitcnt vmcnt(0)" ::: "memory");
.LBB0_429:
	s_or_b64 exec, exec, s[10:11]
	s_waitcnt vmcnt(0)
	buffer_inv sc1
	s_waitcnt vmcnt(0)
.LBB0_430:
	s_or_b64 exec, exec, s[4:5]
	s_waitcnt lgkmcnt(0)
	s_barrier

; __device__ __forceinline__ unsigned xb_ld(unsigned* p)              { return __hip_atomic_load(p, __ATOMIC_RELAXED, __HIP_MEMORY_SCOPE_AGENT); }
; __device__ __forceinline__ unsigned xb_add(unsigned* p, unsigned v) { return __hip_atomic_fetch_add(p, v, __ATOMIC_RELAXED, __HIP_MEMORY_SCOPE_AGENT); }
; #define XB_SPIN(cond, bar) do { unsigned _sp = 0; while (cond) { __builtin_amdgcn_s_sleep(1); \
;     if ((++_sp & 255u) == 0u) { if (xb_ld(&(bar)[XB_TMO])) break; if (_sp > XB_SPIN_CAP) { atomicAdd(&(bar)[XB_TMO], 1u); break; } } } } while (0)
; __device__ __forceinline__ void xcd_barrier(const XcdBarrier& b) {
;     ...
;         const unsigned old = xb_add(&bar[XB_XSUB(b.x)], 1u);
;         const unsigned gen = old / nloc;
;         if (old + 1u == (gen + 1u) * nloc) {
;             __builtin_amdgcn_fence(__ATOMIC_RELEASE, "agent");
;             asm volatile("s_waitcnt vmcnt(0)" ::: "memory");
;             const unsigned og = xb_add(&bar[XB_TOP], 1u);
;             const unsigned tg = og / nx;
;             if (og + 1u == (tg + 1u) * nx) xb_add(&bar[XB_TOPGEN], 1u);
;             else XB_SPIN(xb_ld(&bar[XB_TOPGEN]) == tg, bar);
;             __builtin_amdgcn_fence(__ATOMIC_ACQUIRE, "agent");
;             xb_add(&bar[XB_XGEN(b.x)], 1u);
;             asm volatile("s_waitcnt vmcnt(0)" ::: "memory");
.LBB0_611:
	s_or_b64 exec, exec, s[8:9]
	s_mov_b64 s[8:9], exec
	v_mbcnt_lo_u32_b32 v1, s8, 0
	v_mbcnt_hi_u32_b32 v1, s9, v1
	v_cmp_eq_u32_e32 vcc, 0, v1
	s_and_saveexec_b64 s[10:11], vcc
	s_cbranch_execz .LBB0_613
	s_bcnt1_i32_b64 s3, s[8:9]
	v_mov_b32_e32 v1, 0x2000
	v_mov_b32_e32 v2, s3
	global_atomic_add v1, v2, s[6:7] offset:1024
.LBB0_613:
	s_or_b64 exec, exec, s[10:11]
	s_waitcnt vmcnt(0)
	buffer_inv sc1
	s_waitcnt vmcnt(0)
.LBB0_614:
	s_or_b64 exec, exec, s[4:5]
	s_waitcnt lgkmcnt(0)
	s_barrier

; __device__ __forceinline__ unsigned xb_ld(unsigned* p)              { return __hip_atomic_load(p, __ATOMIC_RELAXED, __HIP_MEMORY_SCOPE_AGENT); }
; __device__ __forceinline__ unsigned xb_add(unsigned* p, unsigned v) { return __hip_atomic_fetch_add(p, v, __ATOMIC_RELAXED, __HIP_MEMORY_SCOPE_AGENT); }
; #define XB_SPIN(cond, bar) do { unsigned _sp = 0; while (cond) { __builtin_amdgcn_s_sleep(1); \
;     if ((++_sp & 255u) == 0u) { if (xb_ld(&(bar)[XB_TMO])) break; if (_sp > XB_SPIN_CAP) { atomicAdd(&(bar)[XB_TMO], 1u); break; } } } } while (0)
; __device__ __forceinline__ void xcd_barrier(const XcdBarrier& b) {
;     ...
;         const unsigned old = xb_add(&bar[XB_XSUB(b.x)], 1u);
;         const unsigned gen = old / nloc;
;         if (old + 1u == (gen + 1u) * nloc) {
;             __builtin_amdgcn_fence(__ATOMIC_RELEASE, "agent");
;             asm volatile("s_waitcnt vmcnt(0)" ::: "memory");
;             const unsigned og = xb_add(&bar[XB_TOP], 1u);
;             const unsigned tg = og / nx;
;             if (og + 1u == (tg + 1u) * nx) xb_add(&bar[XB_TOPGEN], 1u);
;             else XB_SPIN(xb_ld(&bar[XB_TOPGEN]) == tg, bar);
;             __builtin_amdgcn_fence(__ATOMIC_ACQUIRE, "agent");
;             xb_add(&bar[XB_XGEN(b.x)], 1u);
;             asm volatile("s_waitcnt vmcnt(0)" ::: "memory");
.LBB0_743:
	s_or_b64 exec, exec, s[10:11]
	s_waitcnt vmcnt(0)
	buffer_inv sc1
	s_waitcnt vmcnt(0)
.LBB0_744:
	s_or_b64 exec, exec, s[4:5]
	s_waitcnt lgkmcnt(0)
	s_barrier

; __device__ __forceinline__ unsigned xb_ld(unsigned* p)              { return __hip_atomic_load(p, __ATOMIC_RELAXED, __HIP_MEMORY_SCOPE_AGENT); }
; __device__ __forceinline__ unsigned xb_add(unsigned* p, unsigned v) { return __hip_atomic_fetch_add(p, v, __ATOMIC_RELAXED, __HIP_MEMORY_SCOPE_AGENT); }
; #define XB_SPIN(cond, bar) do { unsigned _sp = 0; while (cond) { __builtin_amdgcn_s_sleep(1); \
;     if ((++_sp & 255u) == 0u) { if (xb_ld(&(bar)[XB_TMO])) break; if (_sp > XB_SPIN_CAP) { atomicAdd(&(bar)[XB_TMO], 1u); break; } } } } while (0)
; __device__ __forceinline__ void xcd_barrier(const XcdBarrier& b) {
;     ...
;         const unsigned old = xb_add(&bar[XB_XSUB(b.x)], 1u);
;         const unsigned gen = old / nloc;
;         if (old + 1u == (gen + 1u) * nloc) {
;             __builtin_amdgcn_fence(__ATOMIC_RELEASE, "agent");
;             asm volatile("s_waitcnt vmcnt(0)" ::: "memory");
;             const unsigned og = xb_add(&bar[XB_TOP], 1u);
;             const unsigned tg = og / nx;
;             if (og + 1u == (tg + 1u) * nx) xb_add(&bar[XB_TOPGEN], 1u);
;             else XB_SPIN(xb_ld(&bar[XB_TOPGEN]) == tg, bar);
;             __builtin_amdgcn_fence(__ATOMIC_ACQUIRE, "agent");
;             xb_add(&bar[XB_XGEN(b.x)], 1u);
;             asm volatile("s_waitcnt vmcnt(0)" ::: "memory");
.LBB0_873:
	s_or_b64 exec, exec, s[10:11]
	s_waitcnt vmcnt(0)
	buffer_inv sc1
	s_waitcnt vmcnt(0)
.LBB0_874:
	s_or_b64 exec, exec, s[4:5]
	s_waitcnt lgkmcnt(0)
	s_barrier

; __device__ __forceinline__ unsigned xb_ld(unsigned* p)              { return __hip_atomic_load(p, __ATOMIC_RELAXED, __HIP_MEMORY_SCOPE_AGENT); }
; __device__ __forceinline__ unsigned xb_add(unsigned* p, unsigned v) { return __hip_atomic_fetch_add(p, v, __ATOMIC_RELAXED, __HIP_MEMORY_SCOPE_AGENT); }
; #define XB_SPIN(cond, bar) do { unsigned _sp = 0; while (cond) { __builtin_amdgcn_s_sleep(1); \
;     if ((++_sp & 255u) == 0u) { if (xb_ld(&(bar)[XB_TMO])) break; if (_sp > XB_SPIN_CAP) { atomicAdd(&(bar)[XB_TMO], 1u); break; } } } } while (0)
; __device__ __forceinline__ void xcd_barrier(const XcdBarrier& b) {
;     ...
;         const unsigned old = xb_add(&bar[XB_XSUB(b.x)], 1u);
;         const unsigned gen = old / nloc;
;         if (old + 1u == (gen + 1u) * nloc) {
;             __builtin_amdgcn_fence(__ATOMIC_RELEASE, "agent");
;             asm volatile("s_waitcnt vmcnt(0)" ::: "memory");
;             const unsigned og = xb_add(&bar[XB_TOP], 1u);
;             const unsigned tg = og / nx;
;             if (og + 1u == (tg + 1u) * nx) xb_add(&bar[XB_TOPGEN], 1u);
;             else XB_SPIN(xb_ld(&bar[XB_TOPGEN]) == tg, bar);
;             __builtin_amdgcn_fence(__ATOMIC_ACQUIRE, "agent");
;             xb_add(&bar[XB_XGEN(b.x)], 1u);
;             asm volatile("s_waitcnt vmcnt(0)" ::: "memory");
.LBB0_962:
	s_or_b64 exec, exec, s[10:11]
	s_waitcnt vmcnt(0)
	buffer_inv sc1
	s_waitcnt vmcnt(0)
.LBB0_963:
	s_or_b64 exec, exec, s[4:5]
	s_waitcnt lgkmcnt(0)
	s_barrier

; __device__ __forceinline__ unsigned xb_ld(unsigned* p)              { return __hip_atomic_load(p, __ATOMIC_RELAXED, __HIP_MEMORY_SCOPE_AGENT); }
; __device__ __forceinline__ unsigned xb_add(unsigned* p, unsigned v) { return __hip_atomic_fetch_add(p, v, __ATOMIC_RELAXED, __HIP_MEMORY_SCOPE_AGENT); }
; #define XB_SPIN(cond, bar) do { unsigned _sp = 0; while (cond) { __builtin_amdgcn_s_sleep(1); \
;     if ((++_sp & 255u) == 0u) { if (xb_ld(&(bar)[XB_TMO])) break; if (_sp > XB_SPIN_CAP) { atomicAdd(&(bar)[XB_TMO], 1u); break; } } } } while (0)
; __device__ __forceinline__ void xcd_barrier(const XcdBarrier& b) {
;     ...
;         const unsigned old = xb_add(&bar[XB_XSUB(b.x)], 1u);
;         const unsigned gen = old / nloc;
;         if (old + 1u == (gen + 1u) * nloc) {
;             __builtin_amdgcn_fence(__ATOMIC_RELEASE, "agent");
;             asm volatile("s_waitcnt vmcnt(0)" ::: "memory");
;             const unsigned og = xb_add(&bar[XB_TOP], 1u);
;             const unsigned tg = og / nx;
;             if (og + 1u == (tg + 1u) * nx) xb_add(&bar[XB_TOPGEN], 1u);
;             else XB_SPIN(xb_ld(&bar[XB_TOPGEN]) == tg, bar);
;             __builtin_amdgcn_fence(__ATOMIC_ACQUIRE, "agent");
;             xb_add(&bar[XB_XGEN(b.x)], 1u);
;             asm volatile("s_waitcnt vmcnt(0)" ::: "memory");
.LBB0_1049:
	s_or_b64 exec, exec, s[6:7]
	s_mov_b64 s[6:7], exec
	v_mbcnt_lo_u32_b32 v1, s6, 0
	v_mbcnt_hi_u32_b32 v1, s7, v1
	v_cmp_eq_u32_e32 vcc, 0, v1
	s_and_saveexec_b64 s[8:9], vcc
	s_cbranch_execz .LBB0_1051
	s_bcnt1_i32_b64 s6, s[6:7]
	v_mov_b32_e32 v1, 0x2000
	v_mov_b32_e32 v2, s6
	global_atomic_add v1, v2, s[4:5] offset:1024
.LBB0_1051:
	s_or_b64 exec, exec, s[8:9]
	s_waitcnt vmcnt(0)
	buffer_inv sc1
	s_waitcnt vmcnt(0)
.LBB0_1052:
	s_or_b64 exec, exec, s[2:3]
	s_waitcnt lgkmcnt(0)
	s_barrier

; __device__ __forceinline__ unsigned xb_ld(unsigned* p)              { return __hip_atomic_load(p, __ATOMIC_RELAXED, __HIP_MEMORY_SCOPE_AGENT); }
; __device__ __forceinline__ unsigned xb_add(unsigned* p, unsigned v) { return __hip_atomic_fetch_add(p, v, __ATOMIC_RELAXED, __HIP_MEMORY_SCOPE_AGENT); }
; #define XB_SPIN(cond, bar) do { unsigned _sp = 0; while (cond) { __builtin_amdgcn_s_sleep(1); \
;     if ((++_sp & 255u) == 0u) { if (xb_ld(&(bar)[XB_TMO])) break; if (_sp > XB_SPIN_CAP) { atomicAdd(&(bar)[XB_TMO], 1u); break; } } } } while (0)
; __device__ __forceinline__ void xcd_barrier(const XcdBarrier& b) {
;     ...
;         const unsigned old = xb_add(&bar[XB_XSUB(b.x)], 1u);
;         const unsigned gen = old / nloc;
;         if (old + 1u == (gen + 1u) * nloc) {
;             __builtin_amdgcn_fence(__ATOMIC_RELEASE, "agent");
;             asm volatile("s_waitcnt vmcnt(0)" ::: "memory");
;             const unsigned og = xb_add(&bar[XB_TOP], 1u);
;             const unsigned tg = og / nx;
;             if (og + 1u == (tg + 1u) * nx) xb_add(&bar[XB_TOPGEN], 1u);
;             else XB_SPIN(xb_ld(&bar[XB_TOPGEN]) == tg, bar);
;             __builtin_amdgcn_fence(__ATOMIC_ACQUIRE, "agent");
;             xb_add(&bar[XB_XGEN(b.x)], 1u);
;             asm volatile("s_waitcnt vmcnt(0)" ::: "memory");
.LBB0_1283:
	s_or_b64 exec, exec, s[4:5]
	s_mov_b64 s[4:5], exec
	v_mbcnt_lo_u32_b32 v1, s4, 0
	v_mbcnt_hi_u32_b32 v1, s5, v1
	v_cmp_eq_u32_e32 vcc, 0, v1
	s_and_saveexec_b64 s[8:9], vcc
	s_cbranch_execz .LBB0_1285
	s_bcnt1_i32_b64 s4, s[4:5]
	v_mov_b32_e32 v1, 0
	v_mov_b32_e32 v2, s4
	global_atomic_add v1, v2, s[6:7]
.LBB0_1285:
	s_or_b64 exec, exec, s[8:9]
	s_waitcnt vmcnt(0)
	buffer_inv sc1
	s_waitcnt vmcnt(0)
.LBB0_1286:
	s_or_b64 exec, exec, s[2:3]
	s_waitcnt lgkmcnt(0)
	s_barrier

; __device__ __forceinline__ unsigned xb_ld(unsigned* p)              { return __hip_atomic_load(p, __ATOMIC_RELAXED, __HIP_MEMORY_SCOPE_AGENT); }
; __device__ __forceinline__ unsigned xb_add(unsigned* p, unsigned v) { return __hip_atomic_fetch_add(p, v, __ATOMIC_RELAXED, __HIP_MEMORY_SCOPE_AGENT); }
; #define XB_SPIN(cond, bar) do { unsigned _sp = 0; while (cond) { __builtin_amdgcn_s_sleep(1); \
;     if ((++_sp & 255u) == 0u) { if (xb_ld(&(bar)[XB_TMO])) break; if (_sp > XB_SPIN_CAP) { atomicAdd(&(bar)[XB_TMO], 1u); break; } } } } while (0)
; __device__ __forceinline__ void xcd_barrier(const XcdBarrier& b) {
;     ...
;         const unsigned old = xb_add(&bar[XB_XSUB(b.x)], 1u);
;         const unsigned gen = old / nloc;
;         if (old + 1u == (gen + 1u) * nloc) {
;             __builtin_amdgcn_fence(__ATOMIC_RELEASE, "agent");
;             asm volatile("s_waitcnt vmcnt(0)" ::: "memory");
;             const unsigned og = xb_add(&bar[XB_TOP], 1u);
;             const unsigned tg = og / nx;
;             if (og + 1u == (tg + 1u) * nx) xb_add(&bar[XB_TOPGEN], 1u);
;             else XB_SPIN(xb_ld(&bar[XB_TOPGEN]) == tg, bar);
;             __builtin_amdgcn_fence(__ATOMIC_ACQUIRE, "agent");
;             xb_add(&bar[XB_XGEN(b.x)], 1u);
;             asm volatile("s_waitcnt vmcnt(0)" ::: "memory");
.LBB0_1389:
	s_or_b64 exec, exec, s[8:9]
	s_waitcnt vmcnt(0)
	buffer_inv sc1
	s_waitcnt vmcnt(0)
.LBB0_1390:
	s_or_b64 exec, exec, s[2:3]
	s_waitcnt lgkmcnt(0)
	s_barrier

; __device__ __forceinline__ unsigned xb_ld(unsigned* p)              { return __hip_atomic_load(p, __ATOMIC_RELAXED, __HIP_MEMORY_SCOPE_AGENT); }
; __device__ __forceinline__ unsigned xb_add(unsigned* p, unsigned v) { return __hip_atomic_fetch_add(p, v, __ATOMIC_RELAXED, __HIP_MEMORY_SCOPE_AGENT); }
; #define XB_SPIN(cond, bar) do { unsigned _sp = 0; while (cond) { __builtin_amdgcn_s_sleep(1); \
;     if ((++_sp & 255u) == 0u) { if (xb_ld(&(bar)[XB_TMO])) break; if (_sp > XB_SPIN_CAP) { atomicAdd(&(bar)[XB_TMO], 1u); break; } } } } while (0)
; __device__ __forceinline__ void xcd_barrier(const XcdBarrier& b) {
;     ...
;         const unsigned old = xb_add(&bar[XB_XSUB(b.x)], 1u);
;         const unsigned gen = old / nloc;
;         if (old + 1u == (gen + 1u) * nloc) {
;             __builtin_amdgcn_fence(__ATOMIC_RELEASE, "agent");
;             asm volatile("s_waitcnt vmcnt(0)" ::: "memory");
;             const unsigned og = xb_add(&bar[XB_TOP], 1u);
;             const unsigned tg = og / nx;
;             if (og + 1u == (tg + 1u) * nx) xb_add(&bar[XB_TOPGEN], 1u);
;             else XB_SPIN(xb_ld(&bar[XB_TOPGEN]) == tg, bar);
;             __builtin_amdgcn_fence(__ATOMIC_ACQUIRE, "agent");
;             xb_add(&bar[XB_XGEN(b.x)], 1u);
;             asm volatile("s_waitcnt vmcnt(0)" ::: "memory");
.LBB0_1488:
	s_or_b64 exec, exec, s[8:9]
	s_waitcnt vmcnt(0)
	buffer_inv sc1
	s_waitcnt vmcnt(0)
.LBB0_1489:
	s_or_b64 exec, exec, s[2:3]
	s_waitcnt lgkmcnt(0)
	s_barrier
